# v83 with every lane permute placed at least one instruction behind the op_sel fp8 convert that feeds it (hazard-table row 25 margin); no functional change
# baseline (speedup 1.0000x reference)
.LBB0_868:
	s_nop 15
	s_nop 15
	s_waitcnt vmcnt(0)
	v_pk_mul_f32 v[30:31], v[10:11], s[22:23] op_sel_hi:[1,0]
	s_nop 0
	v_pk_fma_f32 v[32:33], v[158:159], s[24:25], v[30:31] op_sel_hi:[1,0,1]
	v_pk_mul_f32 v[12:13], v[12:13], s[22:23] op_sel_hi:[1,0]
	v_med3_f32 v21, v32, s74, v215
	v_med3_f32 v29, v33, s74, v215
	v_cvt_pk_fp8_f32 v22, v21, v29
	v_pk_mul_f32 v[14:15], v[14:15], s[22:23] op_sel_hi:[1,0]
	v_pk_fma_f32 v[10:11], v[160:161], s[24:25], v[12:13] op_sel_hi:[1,0,1]
	v_pk_fma_f32 v[130:131], v[130:131], s[24:25], v[14:15] op_sel_hi:[1,0,1]
	v_med3_f32 v10, v10, s74, v215
	v_med3_f32 v11, v11, s74, v215
	v_pk_fma_f32 v[154:155], v[154:155], s[24:25], v[14:15] op_sel_hi:[1,0,1]
	v_med3_f32 v130, v130, s74, v215
	v_cvt_pk_fp8_f32 v22, v10, v11 op_sel:[0,0,1]
	v_med3_f32 v10, v131, s74, v215
	ds_bpermute_b32 v22, v250, v22
	v_mov_b32_e32 v29, 0
	v_pk_fma_f32 v[150:151], v[150:151], s[24:25], v[30:31] op_sel_hi:[1,0,1]
	v_pk_fma_f32 v[146:147], v[146:147], s[24:25], v[14:15] op_sel_hi:[1,0,1]
	v_med3_f32 v32, v154, s74, v215
	v_med3_f32 v33, v155, s74, v215
	v_cvt_pk_fp8_f32 v29, v130, v10
	v_pk_mul_f32 v[16:17], v[16:17], s[22:23] op_sel_hi:[1,0]
	v_pk_fma_f32 v[142:143], v[142:143], s[24:25], v[30:31] op_sel_hi:[1,0,1]
	v_pk_fma_f32 v[138:139], v[138:139], s[24:25], v[14:15] op_sel_hi:[1,0,1]
	v_med3_f32 v150, v150, s74, v215
	v_med3_f32 v151, v151, s74, v215
	v_med3_f32 v146, v146, s74, v215
	v_med3_f32 v147, v147, s74, v215
	v_cvt_pk_fp8_f32 v23, v32, v33
	v_pk_fma_f32 v[132:133], v[132:133], s[24:25], v[16:17] op_sel_hi:[1,0,1]
	v_med3_f32 v142, v142, s74, v215
	v_med3_f32 v143, v143, s74, v215
	v_med3_f32 v138, v138, s74, v215
	v_med3_f32 v139, v139, s74, v215
	v_cvt_pk_fp8_f32 v24, v150, v151
	v_cvt_pk_fp8_f32 v25, v146, v147
	v_pk_fma_f32 v[156:157], v[156:157], s[24:25], v[16:17] op_sel_hi:[1,0,1]
	v_cvt_pk_fp8_f32 v26, v142, v143
	v_cvt_pk_fp8_f32 v27, v138, v139
	v_med3_f32 v10, v132, s74, v215
	v_med3_f32 v11, v133, s74, v215
	v_pk_fma_f32 v[152:153], v[152:153], s[24:25], v[12:13] op_sel_hi:[1,0,1]
	v_pk_fma_f32 v[148:149], v[148:149], s[24:25], v[16:17] op_sel_hi:[1,0,1]
	v_med3_f32 v154, v156, s74, v215
	v_med3_f32 v155, v157, s74, v215
	v_cvt_pk_fp8_f32 v29, v10, v11 op_sel:[0,0,1]
	v_or_b32_e32 v10, 48, v20
	ds_bpermute_b32 v29, v250, v29
	v_pk_fma_f32 v[144:145], v[144:145], s[24:25], v[12:13] op_sel_hi:[1,0,1]
	v_pk_fma_f32 v[140:141], v[140:141], s[24:25], v[16:17] op_sel_hi:[1,0,1]
	v_med3_f32 v152, v152, s74, v215
	v_med3_f32 v153, v153, s74, v215
	v_med3_f32 v148, v148, s74, v215
	v_med3_f32 v149, v149, s74, v215
	v_cvt_pk_fp8_f32 v23, v154, v155 op_sel:[0,0,1]
	v_ashrrev_i32_e32 v11, 31, v10
	ds_bpermute_b32 v23, v250, v23
	v_med3_f32 v144, v144, s74, v215
	v_med3_f32 v145, v145, s74, v215
	v_med3_f32 v140, v140, s74, v215
	v_med3_f32 v141, v141, s74, v215
	v_cvt_pk_fp8_f32 v24, v152, v153 op_sel:[0,0,1]
	v_cvt_pk_fp8_f32 v25, v148, v149 op_sel:[0,0,1]
	ds_bpermute_b32 v24, v250, v24
	v_lshlrev_b64 v[10:11], 11, v[10:11]
	ds_bpermute_b32 v25, v250, v25
	v_cvt_pk_fp8_f32 v26, v144, v145 op_sel:[0,0,1]
	v_cvt_pk_fp8_f32 v27, v140, v141 op_sel:[0,0,1]
	ds_bpermute_b32 v26, v250, v26
	v_lshl_add_u64 v[10:11], s[16:17], 0, v[10:11]
	ds_bpermute_b32 v27, v250, v27
	v_lshl_add_u64 v[10:11], v[10:11], 0, v[18:19]
	v_lshl_add_u64 v[10:11], v[10:11], 0, v[202:203]
	v_pk_fma_f32 v[18:19], v[128:129], s[24:25], v[12:13] op_sel_hi:[1,0,1]
	v_pk_fma_f32 v[20:21], v[126:127], s[24:25], v[30:31] op_sel_hi:[1,0,1]
	s_waitcnt lgkmcnt(0)
	global_store_dwordx2 v[4:5], v[22:23], off
	global_store_dwordx2 v[6:7], v[24:25], off
	global_store_dwordx2 v[8:9], v[26:27], off
	v_pk_fma_f32 v[24:25], v[122:123], s[24:25], v[14:15] op_sel_hi:[1,0,1]
	v_med3_f32 v20, v20, s74, v215
	v_med3_f32 v21, v21, s74, v215
	v_med3_f32 v26, v18, s74, v215
	v_mov_b32_e32 v18, 0
	v_med3_f32 v27, v19, s74, v215
	v_cvt_pk_fp8_f32 v18, v20, v21
	v_med3_f32 v20, v24, s74, v215
	v_med3_f32 v21, v25, s74, v215
	v_mov_b32_e32 v19, 0
	v_cvt_pk_fp8_f32 v19, v20, v21
	v_pk_fma_f32 v[22:23], v[124:125], s[24:25], v[16:17] op_sel_hi:[1,0,1]
	v_cvt_pk_fp8_f32 v18, v26, v27 op_sel:[0,0,1]
	v_med3_f32 v20, v22, s74, v215
	ds_bpermute_b32 v18, v250, v18
	v_med3_f32 v21, v23, s74, v215
	v_cvt_pk_fp8_f32 v19, v20, v21 op_sel:[0,0,1]
	v_add_co_u32_e32 v20, vcc, s75, v4
	ds_bpermute_b32 v19, v250, v19
	v_pk_fma_f32 v[24:25], v[114:115], s[24:25], v[14:15] op_sel_hi:[1,0,1]
	s_nop 0
	v_addc_co_u32_e32 v21, vcc, 0, v5, vcc
	s_waitcnt lgkmcnt(0)
	global_store_dwordx2 v[20:21], v[18:19], off
	v_pk_fma_f32 v[18:19], v[120:121], s[24:25], v[12:13] op_sel_hi:[1,0,1]
	v_pk_fma_f32 v[20:21], v[118:119], s[24:25], v[30:31] op_sel_hi:[1,0,1]
	v_med3_f32 v26, v18, s74, v215
	v_med3_f32 v20, v20, s74, v215
	v_med3_f32 v21, v21, s74, v215
	v_mov_b32_e32 v18, 0
	v_med3_f32 v27, v19, s74, v215
	v_cvt_pk_fp8_f32 v18, v20, v21
	v_med3_f32 v20, v24, s74, v215
	v_med3_f32 v21, v25, s74, v215
	v_mov_b32_e32 v19, 0
	v_cvt_pk_fp8_f32 v19, v20, v21
	v_pk_fma_f32 v[22:23], v[116:117], s[24:25], v[16:17] op_sel_hi:[1,0,1]
	v_cvt_pk_fp8_f32 v18, v26, v27 op_sel:[0,0,1]
	v_med3_f32 v20, v22, s74, v215
	ds_bpermute_b32 v18, v250, v18
	v_med3_f32 v21, v23, s74, v215
	v_cvt_pk_fp8_f32 v19, v20, v21 op_sel:[0,0,1]
	v_add_co_u32_e32 v20, vcc, s76, v4
	ds_bpermute_b32 v19, v250, v19
	v_pk_fma_f32 v[24:25], v[106:107], s[24:25], v[14:15] op_sel_hi:[1,0,1]
	s_nop 0
	v_addc_co_u32_e32 v21, vcc, 0, v5, vcc
	s_waitcnt lgkmcnt(0)
	global_store_dwordx2 v[20:21], v[18:19], off
	v_pk_fma_f32 v[18:19], v[112:113], s[24:25], v[12:13] op_sel_hi:[1,0,1]
	v_pk_fma_f32 v[20:21], v[110:111], s[24:25], v[30:31] op_sel_hi:[1,0,1]
	v_med3_f32 v26, v18, s74, v215
	v_med3_f32 v20, v20, s74, v215
	v_med3_f32 v21, v21, s74, v215
	v_mov_b32_e32 v18, 0
	v_med3_f32 v27, v19, s74, v215
	v_cvt_pk_fp8_f32 v18, v20, v21
	v_med3_f32 v20, v24, s74, v215
	v_med3_f32 v21, v25, s74, v215
	v_mov_b32_e32 v19, 0
	v_cvt_pk_fp8_f32 v19, v20, v21
	v_pk_fma_f32 v[22:23], v[108:109], s[24:25], v[16:17] op_sel_hi:[1,0,1]
	v_cvt_pk_fp8_f32 v18, v26, v27 op_sel:[0,0,1]
	v_med3_f32 v20, v22, s74, v215
	ds_bpermute_b32 v18, v250, v18
	v_med3_f32 v21, v23, s74, v215
	v_cvt_pk_fp8_f32 v19, v20, v21 op_sel:[0,0,1]
	v_add_co_u32_e32 v20, vcc, s77, v4
	ds_bpermute_b32 v19, v250, v19
	v_pk_fma_f32 v[136:137], v[136:137], s[24:25], v[12:13] op_sel_hi:[1,0,1]
	s_nop 0
	v_addc_co_u32_e32 v21, vcc, 0, v5, vcc
	v_pk_fma_f32 v[134:135], v[134:135], s[24:25], v[30:31] op_sel_hi:[1,0,1]
	s_waitcnt lgkmcnt(0)
	global_store_dwordx2 v[20:21], v[18:19], off
	v_pk_fma_f32 v[12:13], v[100:101], s[24:25], v[12:13] op_sel_hi:[1,0,1]
	v_pk_fma_f32 v[18:19], v[98:99], s[24:25], v[30:31] op_sel_hi:[1,0,1]
	v_pk_fma_f32 v[14:15], v[90:91], s[24:25], v[14:15] op_sel_hi:[1,0,1]
	v_med3_f32 v134, v134, s74, v215
	v_med3_f32 v135, v135, s74, v215
	v_med3_f32 v18, v18, s74, v215
	v_med3_f32 v19, v19, s74, v215
	v_med3_f32 v20, v12, s74, v215
	v_med3_f32 v21, v13, s74, v215
	v_mov_b32_e32 v12, 0
	v_med3_f32 v14, v14, s74, v215
	v_med3_f32 v15, v15, s74, v215
	v_mov_b32_e32 v13, 0
	v_cvt_pk_fp8_f32 v28, v134, v135
	v_cvt_pk_fp8_f32 v12, v18, v19
	v_cvt_pk_fp8_f32 v13, v14, v15
	v_pk_fma_f32 v[16:17], v[92:93], s[24:25], v[16:17] op_sel_hi:[1,0,1]
	v_med3_f32 v136, v136, s74, v215
	v_med3_f32 v137, v137, s74, v215
	v_med3_f32 v14, v16, s74, v215
	v_med3_f32 v15, v17, s74, v215
	v_cvt_pk_fp8_f32 v28, v136, v137 op_sel:[0,0,1]
	v_cvt_pk_fp8_f32 v12, v20, v21 op_sel:[0,0,1]
	ds_bpermute_b32 v28, v250, v28
	v_cvt_pk_fp8_f32 v13, v14, v15 op_sel:[0,0,1]
	ds_bpermute_b32 v12, v250, v12
	v_add_co_u32_e32 v14, vcc, s78, v4
	ds_bpermute_b32 v13, v250, v13
	s_waitcnt lgkmcnt(0)
	global_store_dwordx2 v[10:11], v[28:29], off
	s_nop 0
	v_addc_co_u32_e32 v15, vcc, 0, v5, vcc
	s_waitcnt lgkmcnt(0)
	global_store_dwordx2 v[14:15], v[12:13], off
	v_lshl_add_u64 v[2:3], v[4:5], 0, s[12:13]
	v_lshl_add_u64 v[20:21], v[4:5], 0, s[26:27]
	v_lshl_add_u64 v[22:23], v[4:5], 0, s[28:29]
	v_lshl_add_u64 v[24:25], v[4:5], 0, s[30:31]
	s_andn2_b64 vcc, exec, s[98:99]
	v_pk_mul_f32 v[14:15], v[194:195], s[22:23] op_sel_hi:[1,0]
	v_pk_mul_f32 v[12:13], v[192:193], s[22:23] op_sel_hi:[1,0]
	v_pk_mul_f32 v[16:17], v[196:197], s[22:23] op_sel_hi:[1,0]
	v_pk_fma_f32 v[26:27], v[104:105], s[24:25], v[14:15] op_sel_hi:[1,0,1]
	v_pk_fma_f32 v[28:29], v[102:103], s[24:25], v[12:13] op_sel_hi:[1,0,1]
	v_pk_fma_f32 v[32:33], v[94:95], s[24:25], v[16:17] op_sel_hi:[1,0,1]
	v_med3_f32 v28, v28, s74, v215
	v_med3_f32 v29, v29, s74, v215
	v_med3_f32 v90, v26, s74, v215
	v_mov_b32_e32 v26, 0
	v_med3_f32 v91, v27, s74, v215
	v_cvt_pk_fp8_f32 v26, v28, v29
	v_med3_f32 v28, v32, s74, v215
	v_med3_f32 v29, v33, s74, v215
	v_mov_b32_e32 v27, 0
	v_cvt_pk_fp8_f32 v27, v28, v29
	v_pk_mul_f32 v[18:19], v[198:199], s[22:23] op_sel_hi:[1,0]
	v_pk_fma_f32 v[82:83], v[82:83], s[24:25], v[16:17] op_sel_hi:[1,0,1]
	v_pk_fma_f32 v[30:31], v[96:97], s[24:25], v[18:19] op_sel_hi:[1,0,1]
	v_pk_fma_f32 v[32:33], v[84:85], s[24:25], v[18:19] op_sel_hi:[1,0,1]
	v_med3_f32 v28, v30, s74, v215
	v_med3_f32 v29, v31, s74, v215
	v_cvt_pk_fp8_f32 v27, v28, v29 op_sel:[0,0,1]
	v_pk_fma_f32 v[28:29], v[88:89], s[24:25], v[14:15] op_sel_hi:[1,0,1]
	ds_bpermute_b32 v27, v250, v27
	v_pk_fma_f32 v[30:31], v[86:87], s[24:25], v[12:13] op_sel_hi:[1,0,1]
	v_med3_f32 v84, v28, s74, v215
	v_med3_f32 v30, v30, s74, v215
	v_med3_f32 v31, v31, s74, v215
	v_mov_b32_e32 v28, 0
	v_med3_f32 v85, v29, s74, v215
	v_cvt_pk_fp8_f32 v28, v30, v31
	v_med3_f32 v30, v82, s74, v215
	v_med3_f32 v31, v83, s74, v215
	v_mov_b32_e32 v29, 0
	v_cvt_pk_fp8_f32 v29, v30, v31
	v_med3_f32 v30, v32, s74, v215
	v_med3_f32 v31, v33, s74, v215
	v_pk_fma_f32 v[32:33], v[78:79], s[24:25], v[12:13] op_sel_hi:[1,0,1]
	v_cvt_pk_fp8_f32 v29, v30, v31 op_sel:[0,0,1]
	v_pk_fma_f32 v[30:31], v[80:81], s[24:25], v[14:15] op_sel_hi:[1,0,1]
	ds_bpermute_b32 v29, v250, v29
	v_pk_fma_f32 v[74:75], v[74:75], s[24:25], v[16:17] op_sel_hi:[1,0,1]
	v_med3_f32 v32, v32, s74, v215
	v_med3_f32 v33, v33, s74, v215
	v_med3_f32 v78, v30, s74, v215
	v_mov_b32_e32 v30, 0
	v_med3_f32 v79, v31, s74, v215
	v_cvt_pk_fp8_f32 v30, v32, v33
	v_med3_f32 v32, v74, s74, v215
	v_med3_f32 v33, v75, s74, v215
	v_mov_b32_e32 v31, 0
	v_cvt_pk_fp8_f32 v31, v32, v33
	v_pk_fma_f32 v[76:77], v[76:77], s[24:25], v[18:19] op_sel_hi:[1,0,1]
	v_pk_fma_f32 v[70:71], v[70:71], s[24:25], v[12:13] op_sel_hi:[1,0,1]
	v_med3_f32 v32, v76, s74, v215
	v_med3_f32 v33, v77, s74, v215
	v_cvt_pk_fp8_f32 v31, v32, v33 op_sel:[0,0,1]
	v_pk_fma_f32 v[32:33], v[72:73], s[24:25], v[14:15] op_sel_hi:[1,0,1]
	ds_bpermute_b32 v31, v250, v31
	v_pk_fma_f32 v[66:67], v[66:67], s[24:25], v[16:17] op_sel_hi:[1,0,1]
	v_med3_f32 v70, v70, s74, v215
	v_med3_f32 v71, v71, s74, v215
	v_med3_f32 v72, v32, s74, v215
	v_med3_f32 v73, v33, s74, v215
	v_mov_b32_e32 v32, 0
	v_med3_f32 v66, v66, s74, v215
	v_med3_f32 v67, v67, s74, v215
	v_mov_b32_e32 v33, 0
	v_cvt_pk_fp8_f32 v32, v70, v71
	v_cvt_pk_fp8_f32 v33, v66, v67
	v_cvt_pk_fp8_f32 v26, v90, v91 op_sel:[0,0,1]
	v_cvt_pk_fp8_f32 v28, v84, v85 op_sel:[0,0,1]
	ds_bpermute_b32 v26, v250, v26
	v_pk_fma_f32 v[68:69], v[68:69], s[24:25], v[18:19] op_sel_hi:[1,0,1]
	ds_bpermute_b32 v28, v250, v28
	v_cvt_pk_fp8_f32 v30, v78, v79 op_sel:[0,0,1]
	v_med3_f32 v66, v68, s74, v215
	ds_bpermute_b32 v30, v250, v30
	v_med3_f32 v67, v69, s74, v215
	v_cvt_pk_fp8_f32 v32, v72, v73 op_sel:[0,0,1]
	v_cvt_pk_fp8_f32 v33, v66, v67 op_sel:[0,0,1]
	ds_bpermute_b32 v32, v250, v32
	s_nop 0
	ds_bpermute_b32 v33, v250, v33
	s_waitcnt lgkmcnt(0)
	global_store_dwordx2 v[4:5], v[26:27], off offset:128
	global_store_dwordx2 v[6:7], v[28:29], off offset:128
	global_store_dwordx2 v[8:9], v[30:31], off offset:128
	global_store_dwordx2 v[10:11], v[32:33], off offset:128
	v_pk_fma_f32 v[4:5], v[64:65], s[24:25], v[14:15] op_sel_hi:[1,0,1]
	v_pk_fma_f32 v[6:7], v[62:63], s[24:25], v[12:13] op_sel_hi:[1,0,1]
	v_pk_fma_f32 v[10:11], v[58:59], s[24:25], v[16:17] op_sel_hi:[1,0,1]
	v_med3_f32 v6, v6, s74, v215
	v_med3_f32 v7, v7, s74, v215
	v_med3_f32 v26, v4, s74, v215
	v_mov_b32_e32 v4, 0
	v_med3_f32 v27, v5, s74, v215
	v_cvt_pk_fp8_f32 v4, v6, v7
	v_med3_f32 v6, v10, s74, v215
	v_med3_f32 v7, v11, s74, v215
	v_mov_b32_e32 v5, 0
	v_cvt_pk_fp8_f32 v5, v6, v7
	v_pk_fma_f32 v[8:9], v[60:61], s[24:25], v[18:19] op_sel_hi:[1,0,1]
	v_cvt_pk_fp8_f32 v4, v26, v27 op_sel:[0,0,1]
	v_med3_f32 v6, v8, s74, v215
	ds_bpermute_b32 v4, v250, v4
	v_med3_f32 v7, v9, s74, v215
	v_cvt_pk_fp8_f32 v5, v6, v7 op_sel:[0,0,1]
	v_pk_fma_f32 v[6:7], v[56:57], s[24:25], v[14:15] op_sel_hi:[1,0,1]
	ds_bpermute_b32 v5, v250, v5
	v_pk_fma_f32 v[8:9], v[54:55], s[24:25], v[12:13] op_sel_hi:[1,0,1]
	v_pk_fma_f32 v[26:27], v[50:51], s[24:25], v[16:17] op_sel_hi:[1,0,1]
	v_med3_f32 v8, v8, s74, v215
	v_med3_f32 v9, v9, s74, v215
	v_med3_f32 v28, v6, s74, v215
	v_mov_b32_e32 v6, 0
	v_med3_f32 v29, v7, s74, v215
	v_cvt_pk_fp8_f32 v6, v8, v9
	v_med3_f32 v8, v26, s74, v215
	v_med3_f32 v9, v27, s74, v215
	v_mov_b32_e32 v7, 0
	v_cvt_pk_fp8_f32 v7, v8, v9
	v_pk_fma_f32 v[10:11], v[52:53], s[24:25], v[18:19] op_sel_hi:[1,0,1]
	v_cvt_pk_fp8_f32 v6, v28, v29 op_sel:[0,0,1]
	v_med3_f32 v8, v10, s74, v215
	ds_bpermute_b32 v6, v250, v6
	v_med3_f32 v9, v11, s74, v215
	v_cvt_pk_fp8_f32 v7, v8, v9 op_sel:[0,0,1]
	v_pk_fma_f32 v[8:9], v[48:49], s[24:25], v[14:15] op_sel_hi:[1,0,1]
	ds_bpermute_b32 v7, v250, v7
	v_pk_fma_f32 v[10:11], v[46:47], s[24:25], v[12:13] op_sel_hi:[1,0,1]
	v_pk_fma_f32 v[28:29], v[42:43], s[24:25], v[16:17] op_sel_hi:[1,0,1]
	v_med3_f32 v10, v10, s74, v215
	v_med3_f32 v11, v11, s74, v215
	v_med3_f32 v30, v8, s74, v215
	v_mov_b32_e32 v8, 0
	v_med3_f32 v31, v9, s74, v215
	v_cvt_pk_fp8_f32 v8, v10, v11
	v_med3_f32 v10, v28, s74, v215
	v_med3_f32 v11, v29, s74, v215
	v_mov_b32_e32 v9, 0
	v_cvt_pk_fp8_f32 v9, v10, v11
	v_pk_fma_f32 v[26:27], v[44:45], s[24:25], v[18:19] op_sel_hi:[1,0,1]
	v_pk_fma_f32 v[12:13], v[38:39], s[24:25], v[12:13] op_sel_hi:[1,0,1]
	v_med3_f32 v10, v26, s74, v215
	v_med3_f32 v11, v27, s74, v215
	v_cvt_pk_fp8_f32 v9, v10, v11 op_sel:[0,0,1]
	v_pk_fma_f32 v[10:11], v[40:41], s[24:25], v[14:15] op_sel_hi:[1,0,1]
	ds_bpermute_b32 v9, v250, v9
	v_pk_fma_f32 v[14:15], v[36:37], s[24:25], v[18:19] op_sel_hi:[1,0,1]
	v_pk_fma_f32 v[16:17], v[34:35], s[24:25], v[16:17] op_sel_hi:[1,0,1]
	v_med3_f32 v12, v12, s74, v215
	v_med3_f32 v13, v13, s74, v215
	v_med3_f32 v18, v10, s74, v215
	v_mov_b32_e32 v10, 0
	v_med3_f32 v19, v11, s74, v215
	v_cvt_pk_fp8_f32 v10, v12, v13
	v_med3_f32 v12, v16, s74, v215
	v_med3_f32 v13, v17, s74, v215
	v_mov_b32_e32 v11, 0
	v_cvt_pk_fp8_f32 v11, v12, v13
	v_cvt_pk_fp8_f32 v8, v30, v31 op_sel:[0,0,1]
	v_med3_f32 v12, v14, s74, v215
	ds_bpermute_b32 v8, v250, v8
	v_med3_f32 v13, v15, s74, v215
	v_cvt_pk_fp8_f32 v10, v18, v19 op_sel:[0,0,1]
	v_cvt_pk_fp8_f32 v11, v12, v13 op_sel:[0,0,1]
	ds_bpermute_b32 v10, v250, v10
	s_nop 0
	ds_bpermute_b32 v11, v250, v11
	s_waitcnt lgkmcnt(0)
	global_store_dwordx2 v[2:3], v[4:5], off offset:128
	global_store_dwordx2 v[20:21], v[6:7], off offset:128
	global_store_dwordx2 v[22:23], v[8:9], off offset:128
	global_store_dwordx2 v[24:25], v[10:11], off offset:128
	s_cbranch_vccnz .LBB0_871
	s_branch .Lp7_entry_pre
